# v34: v33 + MLA softmax: redundant canonicalising v_max (x,x) removed (5 VALU fewer per key-tile pair)
# baseline (speedup 1.0000x reference)
.LBB0_946:
	s_sub_i32 s1, s37, 94
	s_cmp_gt_i32 s1, s35
	s_cbranch_scc1 .Lmla_qkskip1
	s_lshl_b32 s50, s0, 14
	s_add_i32 s1, s50, 0
	v_add_u32_e32 v210, s1, v202
	ds_read_b128 v[98:101], v210 offset:49152
	ds_read_b128 v[102:105], v210 offset:57344
	v_xor_b32_e32 v210, 0x80, v210
	v_max_f32_e32 v186, v66, v67
	s_waitcnt lgkmcnt(1)
	v_mfma_f32_32x32x16_bf16 v[114:129], v[98:101], v[130:133], 0
	v_add_u32_e32 v212, s1, v207
	v_max3_f32 v186, v186, v68, v69
	ds_read_b128 v[178:181], v212 offset:49152
	ds_read_b128 v[182:185], v212 offset:57344
	v_xor_b32_e32 v212, 0x80, v212
	v_max3_f32 v186, v186, v70, v71
	v_max3_f32 v186, v186, v72, v73
	v_max3_f32 v186, v186, v74, v75
	v_max3_f32 v186, v186, v76, v77
	s_waitcnt lgkmcnt(2)
	v_mfma_f32_32x32x16_bf16 v[98:113], v[102:105], v[130:133], 0
	v_max3_f32 v186, v186, v78, v79
	v_lshl_add_u32 v211, s0, 13, v225
	v_max3_f32 v213, v186, v80, v81
	s_waitcnt lgkmcnt(1)
	v_mfma_f32_32x32x16_bf16 v[114:129], v[178:181], v[134:137], v[114:129]
	v_max3_f32 v178, v213, v82, v83
	v_max3_f32 v178, v178, v84, v85
	v_max3_f32 v178, v178, v86, v87
	v_max3_f32 v178, v178, v88, v89
	v_max3_f32 v178, v178, v90, v91
	v_max3_f32 v178, v178, v92, v93
	v_max3_f32 v178, v178, v94, v95
	v_max3_f32 v178, v178, v96, v97
	v_mov_b32_e32 v179, v178
	s_nop 1
	v_permlane32_swap_b32_e32 v178, v179
	v_max_f32_e32 v178, v178, v179
	v_sub_f32_e32 v179, v178, v231
	v_mul_f32_e32 v179, 0x3d93cd3a, v179
	v_cmp_ge_f32_e32 vcc, s36, v179
	s_cmp_eq_u64 vcc, exec
	v_max_f32_e32 v179, v231, v231
	s_waitcnt lgkmcnt(0)
	v_mfma_f32_32x32x16_bf16 v[98:113], v[182:185], v[134:137], v[98:113]
	s_cselect_b64 vcc, -1, 0
	v_max_f32_e32 v178, v179, v178
	v_cndmask_b32_e32 v232, v178, v231, vcc
	v_add_u32_e32 v218, s1, v209
	v_sub_f32_e32 v178, v231, v232
	ds_read_b128 v[186:189], v218 offset:49152
	ds_read_b128 v[190:193], v218 offset:57344
	v_xor_b32_e32 v218, 0x80, v218
	v_mul_f32_e32 v178, 0x3dd53b94, v178
	v_exp_f32_e32 v231, v178
	v_mul_f32_e32 v213, 0xbdd53b94, v232
	v_fmamk_f32 v66, v66, 0x3dd53b94, v213
	s_waitcnt lgkmcnt(1)
	v_mfma_f32_32x32x16_bf16 v[114:129], v[186:189], v[138:141], v[114:129]
	v_exp_f32_e32 v66, v66
	v_fmamk_f32 v82, v82, 0x3dd53b94, v213
	v_add_u32_e32 v219, s1, v224
	v_exp_f32_e32 v82, v82
	v_fmamk_f32 v67, v67, 0x3dd53b94, v213
	ds_read_b128 v[178:181], v219 offset:49152
	ds_read_b128 v[182:185], v219 offset:57344
	v_xor_b32_e32 v219, 0x80, v219
	v_exp_f32_e32 v67, v67
	s_waitcnt lgkmcnt(2)
	v_mfma_f32_32x32x16_bf16 v[98:113], v[190:193], v[138:141], v[98:113]
	v_fmamk_f32 v83, v83, 0x3dd53b94, v213
	v_exp_f32_e32 v83, v83
	v_add_f32_e32 v186, 0, v66
	v_add_f32_e32 v186, v82, v186
	v_add_f32_e32 v186, v67, v186
	v_add_f32_e32 v220, v83, v186
	v_fmamk_f32 v68, v68, 0x3dd53b94, v213
	s_waitcnt lgkmcnt(1)
	v_mfma_f32_32x32x16_bf16 v[114:129], v[178:181], v[142:145], v[114:129]
	v_exp_f32_e32 v68, v68
	v_fmamk_f32 v84, v84, 0x3dd53b94, v213
	v_exp_f32_e32 v84, v84
	v_fmamk_f32 v69, v69, 0x3dd53b94, v213
	ds_read_b128 v[186:189], v210 offset:49152
	ds_read_b128 v[190:193], v210 offset:57344
	v_exp_f32_e32 v69, v69
	v_fmamk_f32 v85, v85, 0x3dd53b94, v213
	s_waitcnt lgkmcnt(2)
	v_mfma_f32_32x32x16_bf16 v[98:113], v[182:185], v[142:145], v[98:113]
	v_exp_f32_e32 v85, v85
	v_add_f32_e32 v178, v68, v220
	v_add_f32_e32 v178, v84, v178
	v_add_f32_e32 v178, v69, v178
	v_add_f32_e32 v210, v85, v178
	v_fmamk_f32 v70, v70, 0x3dd53b94, v213
	s_waitcnt lgkmcnt(1)
	v_mfma_f32_32x32x16_bf16 v[114:129], v[186:189], v[146:149], v[114:129]
	v_exp_f32_e32 v70, v70
	v_fmamk_f32 v86, v86, 0x3dd53b94, v213
	v_exp_f32_e32 v86, v86
	v_fmamk_f32 v71, v71, 0x3dd53b94, v213
	ds_read_b128 v[178:181], v212 offset:49152
	ds_read_b128 v[182:185], v212 offset:57344
	v_exp_f32_e32 v71, v71
	v_fmamk_f32 v87, v87, 0x3dd53b94, v213
	s_waitcnt lgkmcnt(2)
	v_mfma_f32_32x32x16_bf16 v[98:113], v[190:193], v[146:149], v[98:113]
	v_exp_f32_e32 v87, v87
	v_add_f32_e32 v186, v70, v210
	v_add_f32_e32 v186, v86, v186
	v_add_f32_e32 v186, v71, v186
	v_add_f32_e32 v210, v87, v186
	v_fmamk_f32 v72, v72, 0x3dd53b94, v213
	s_waitcnt lgkmcnt(1)
	v_mfma_f32_32x32x16_bf16 v[114:129], v[178:181], v[150:153], v[114:129]
	v_exp_f32_e32 v72, v72
	v_fmamk_f32 v88, v88, 0x3dd53b94, v213
	v_exp_f32_e32 v88, v88
	v_fmamk_f32 v73, v73, 0x3dd53b94, v213
	ds_read_b128 v[186:189], v218 offset:49152
	ds_read_b128 v[190:193], v218 offset:57344
	v_exp_f32_e32 v73, v73
	v_fmamk_f32 v89, v89, 0x3dd53b94, v213
	s_waitcnt lgkmcnt(2)
	v_mfma_f32_32x32x16_bf16 v[98:113], v[182:185], v[150:153], v[98:113]
	v_exp_f32_e32 v89, v89
	v_add_f32_e32 v178, v72, v210
	v_add_f32_e32 v178, v88, v178
	v_add_f32_e32 v178, v73, v178
	v_add_f32_e32 v210, v89, v178
	v_fmamk_f32 v74, v74, 0x3dd53b94, v213
	v_exp_f32_e32 v74, v74
	v_fmamk_f32 v90, v90, 0x3dd53b94, v213
	s_waitcnt lgkmcnt(1)
	v_mfma_f32_32x32x16_bf16 v[114:129], v[186:189], v[154:157], v[114:129]
	v_exp_f32_e32 v90, v90
	v_fmamk_f32 v75, v75, 0x3dd53b94, v213
	v_exp_f32_e32 v75, v75
	v_fmamk_f32 v91, v91, 0x3dd53b94, v213
	ds_read_b128 v[178:181], v219 offset:49152
	ds_read_b128 v[182:185], v219 offset:57344
	v_exp_f32_e32 v91, v91
	v_add_f32_e32 v186, v74, v210
	s_waitcnt lgkmcnt(2)
	v_mfma_f32_32x32x16_bf16 v[98:113], v[190:193], v[154:157], v[98:113]
	v_add_f32_e32 v186, v90, v186
	v_add_f32_e32 v186, v75, v186
	v_add_f32_e32 v190, v91, v186
	v_fmamk_f32 v76, v76, 0x3dd53b94, v213
	v_exp_f32_e32 v76, v76
	v_fmamk_f32 v92, v92, 0x3dd53b94, v213
	s_waitcnt lgkmcnt(1)
	v_mfma_f32_32x32x16_bf16 v[114:129], v[178:181], v[158:161], v[114:129]
	v_exp_f32_e32 v92, v92
	v_fmamk_f32 v77, v77, 0x3dd53b94, v213
	v_add_u32_e32 v186, v211, v226
	v_exp_f32_e32 v77, v77
	v_fmamk_f32 v93, v93, 0x3dd53b94, v213
	ds_read_b128 v[178:181], v186
	ds_read_b128 v[186:189], v186 offset:4096
	v_exp_f32_e32 v93, v93
	s_waitcnt lgkmcnt(2)
	v_mfma_f32_32x32x16_bf16 v[98:113], v[182:185], v[158:161], v[98:113]
	v_add_f32_e32 v190, v76, v190
	v_add_f32_e32 v190, v92, v190
	v_add_f32_e32 v182, v77, v190
	v_add_f32_e32 v190, v93, v182
	v_fmamk_f32 v78, v78, 0x3dd53b94, v213
	v_exp_f32_e32 v78, v78
	v_fmamk_f32 v94, v94, 0x3dd53b94, v213
	s_waitcnt lgkmcnt(1)
	v_mfma_f32_32x32x16_bf16 v[114:129], v[178:181], v[162:165], v[114:129]
	v_exp_f32_e32 v94, v94
	v_fmamk_f32 v79, v79, 0x3dd53b94, v213
	v_add_u32_e32 v182, v211, v206
	v_exp_f32_e32 v79, v79
	v_fmamk_f32 v95, v95, 0x3dd53b94, v213
	ds_read_b128 v[178:181], v182
	ds_read_b128 v[182:185], v182 offset:4096
	v_exp_f32_e32 v95, v95
	s_waitcnt lgkmcnt(2)
	v_mfma_f32_32x32x16_bf16 v[98:113], v[186:189], v[162:165], v[98:113]
	v_add_f32_e32 v190, v78, v190
	v_add_f32_e32 v190, v94, v190
	v_add_f32_e32 v186, v79, v190
	v_add_f32_e32 v190, v95, v186
	v_fmamk_f32 v80, v80, 0x3dd53b94, v213
	v_exp_f32_e32 v80, v80
	v_fmamk_f32 v96, v96, 0x3dd53b94, v213
	s_waitcnt lgkmcnt(1)
	v_mfma_f32_32x32x16_bf16 v[114:129], v[178:181], v[166:169], v[114:129]
	v_exp_f32_e32 v96, v96
	v_fmamk_f32 v81, v81, 0x3dd53b94, v213
	v_add_u32_e32 v186, v211, v208
	v_exp_f32_e32 v81, v81
	v_fmac_f32_e32 v213, 0x3dd53b94, v97
	ds_read_b128 v[178:181], v186
	ds_read_b128 v[186:189], v186 offset:4096
	v_exp_f32_e32 v97, v213
	s_waitcnt lgkmcnt(2)
	v_mfma_f32_32x32x16_bf16 v[98:113], v[182:185], v[166:169], v[98:113]
	v_add_f32_e32 v190, v80, v190
	v_add_f32_e32 v190, v96, v190
	v_add_f32_e32 v182, v81, v190
	v_add_f32_e32 v233, v97, v182
	s_waitcnt lgkmcnt(1)
	v_mfma_f32_32x32x16_bf16 v[114:129], v[178:181], v[170:173], v[114:129]
	v_add_u32_e32 v182, v211, v223
	ds_read_b128 v[190:193], v182
	ds_read_b128 v[236:239], v182 offset:4096
	v_mov_b32_e32 v234, v233
	v_cvt_pk_bf16_f32 v178, v66, v67
	v_cvt_pk_bf16_f32 v179, v68, v69
	v_cvt_pk_bf16_f32 v180, v70, v71
	v_cvt_pk_bf16_f32 v181, v72, v73
	s_waitcnt lgkmcnt(2)
	v_mfma_f32_32x32x16_bf16 v[98:113], v[186:189], v[170:173], v[98:113]
	v_cvt_pk_bf16_f32 v182, v74, v75
	v_cvt_pk_bf16_f32 v183, v76, v77
	v_cvt_pk_bf16_f32 v184, v78, v79
	v_cvt_pk_bf16_f32 v185, v80, v81
	v_permlane32_swap_b32_e32 v233, v234
	v_permlane32_swap_b32_e32 v178, v180
	v_permlane32_swap_b32_e32 v179, v181
	v_permlane32_swap_b32_e32 v182, v184
	v_permlane32_swap_b32_e32 v183, v185
	s_waitcnt lgkmcnt(1)
	v_mfma_f32_32x32x16_bf16 v[114:129], v[190:193], v[174:177], v[114:129]
	v_cvt_pk_bf16_f32 v186, v82, v83
	v_cvt_pk_bf16_f32 v187, v84, v85
	v_cvt_pk_bf16_f32 v188, v86, v87
	v_cvt_pk_bf16_f32 v189, v88, v89
	v_cvt_pk_bf16_f32 v190, v90, v91
	v_cvt_pk_bf16_f32 v191, v92, v93
	v_cvt_pk_bf16_f32 v192, v94, v95
	s_waitcnt lgkmcnt(0)
	v_mfma_f32_32x32x16_bf16 v[98:113], v[236:239], v[174:177], v[98:113]
	v_cvt_pk_bf16_f32 v193, v96, v97
	v_permlane32_swap_b32_e32 v186, v188
	v_permlane32_swap_b32_e32 v187, v189
	v_permlane32_swap_b32_e32 v190, v192
	v_permlane32_swap_b32_e32 v191, v193

.LBB0_958:
	s_lshl_b32 s0, s48, 14
	s_add_i32 s0, s0, 0
	v_add_u32_e32 v210, s0, v202
	ds_read_b128 v[66:69], v210 offset:49152
	ds_read_b128 v[82:85], v210 offset:57344
	v_xor_b32_e32 v210, 0x80, v210
	v_max_f32_e32 v86, v237, v236
	v_max3_f32 v86, v86, v116, v117
	v_max3_f32 v86, v86, v118, v119
	v_max3_f32 v186, v86, v120, v121
	v_add_u32_e32 v212, s0, v207
	ds_read_b128 v[178:181], v212 offset:49152
	ds_read_b128 v[182:185], v212 offset:57344
	v_xor_b32_e32 v212, 0x80, v212
	v_max3_f32 v186, v186, v122, v123
	s_waitcnt lgkmcnt(3)
	v_mfma_f32_32x32x16_bf16 v[66:81], v[66:69], v[130:133], 0
	v_max3_f32 v186, v186, v124, v125
	v_max3_f32 v186, v186, v126, v127
	v_lshl_add_u32 v211, s48, 13, v225
	v_max3_f32 v213, v186, v128, v129
	s_waitcnt lgkmcnt(2)
	v_mfma_f32_32x32x16_bf16 v[82:97], v[82:85], v[130:133], 0
	s_waitcnt lgkmcnt(1)
	v_mfma_f32_32x32x16_bf16 v[66:81], v[178:181], v[134:137], v[66:81]
	v_max3_f32 v178, v213, v98, v99
	v_max3_f32 v178, v178, v100, v101
	v_max3_f32 v178, v178, v102, v103
	v_max3_f32 v178, v178, v104, v105
	v_max3_f32 v178, v178, v106, v107
	v_max3_f32 v178, v178, v108, v109
	v_max3_f32 v178, v178, v110, v111
	v_max3_f32 v178, v178, v112, v113
	v_mov_b32_e32 v179, v178
	s_nop 1
	v_permlane32_swap_b32_e32 v178, v179
	v_max_f32_e32 v178, v178, v179
	v_sub_f32_e32 v179, v178, v232
	v_mul_f32_e32 v179, 0x3d93cd3a, v179
	v_cmp_ge_f32_e32 vcc, s36, v179
	s_cmp_eq_u64 vcc, exec
	s_waitcnt lgkmcnt(0)
	v_mfma_f32_32x32x16_bf16 v[82:97], v[182:185], v[134:137], v[82:97]
	s_cselect_b64 vcc, -1, 0
	v_max_f32_e32 v178, v235, v178
	v_cndmask_b32_e32 v231, v178, v232, vcc
	v_add_u32_e32 v218, s0, v209
	v_sub_f32_e32 v178, v232, v231
	ds_read_b128 v[186:189], v218 offset:49152
	ds_read_b128 v[190:193], v218 offset:57344
	v_xor_b32_e32 v218, 0x80, v218
	v_mul_f32_e32 v178, 0x3dd53b94, v178
	v_exp_f32_e32 v234, v178
	v_mul_f32_e32 v213, 0xbdd53b94, v231
	v_fmamk_f32 v114, v114, 0x3dd53b94, v213
	s_waitcnt lgkmcnt(1)
	v_mfma_f32_32x32x16_bf16 v[66:81], v[186:189], v[138:141], v[66:81]
	v_exp_f32_e32 v220, v114
	v_fmamk_f32 v98, v98, 0x3dd53b94, v213
	v_add_u32_e32 v219, s0, v224
	v_exp_f32_e32 v221, v98
	v_fmamk_f32 v114, v115, 0x3dd53b94, v213
	ds_read_b128 v[178:181], v219 offset:49152
	ds_read_b128 v[182:185], v219 offset:57344
	v_xor_b32_e32 v219, 0x80, v219
	v_exp_f32_e32 v232, v114
	s_waitcnt lgkmcnt(2)
	v_mfma_f32_32x32x16_bf16 v[82:97], v[190:193], v[138:141], v[82:97]
	v_fmamk_f32 v99, v99, 0x3dd53b94, v213
	v_exp_f32_e32 v235, v99
	v_add_f32_e32 v98, 0, v220
	v_add_f32_e32 v98, v221, v98
	v_add_f32_e32 v98, v232, v98
	v_add_f32_e32 v98, v235, v98
	v_fmamk_f32 v99, v116, 0x3dd53b94, v213
	ds_read_b128 v[186:189], v210 offset:49152
	ds_read_b128 v[190:193], v210 offset:57344
	v_exp_f32_e32 v210, v99
	v_fmamk_f32 v99, v100, 0x3dd53b94, v213
	s_waitcnt lgkmcnt(3)
	v_mfma_f32_32x32x16_bf16 v[66:81], v[178:181], v[142:145], v[66:81]
	v_exp_f32_e32 v236, v99
	v_fmamk_f32 v99, v117, 0x3dd53b94, v213
	v_exp_f32_e32 v237, v99
	v_fmamk_f32 v99, v101, 0x3dd53b94, v213
	v_exp_f32_e32 v238, v99
	v_add_f32_e32 v98, v210, v98
	v_add_f32_e32 v98, v236, v98
	s_waitcnt lgkmcnt(2)
	v_mfma_f32_32x32x16_bf16 v[82:97], v[182:185], v[142:145], v[82:97]
	v_add_f32_e32 v98, v237, v98
	v_add_f32_e32 v178, v238, v98
	v_fmamk_f32 v118, v118, 0x3dd53b94, v213
	s_waitcnt lgkmcnt(1)
	v_mfma_f32_32x32x16_bf16 v[66:81], v[186:189], v[146:149], v[66:81]
	v_exp_f32_e32 v118, v118
	v_fmamk_f32 v102, v102, 0x3dd53b94, v213
	ds_read_b128 v[98:101], v212 offset:49152
	ds_read_b128 v[114:117], v212 offset:57344
	v_exp_f32_e32 v212, v102
	v_fmamk_f32 v119, v119, 0x3dd53b94, v213
	v_exp_f32_e32 v119, v119
	v_fmamk_f32 v103, v103, 0x3dd53b94, v213
	s_waitcnt lgkmcnt(2)
	v_mfma_f32_32x32x16_bf16 v[82:97], v[190:193], v[146:149], v[82:97]
	v_exp_f32_e32 v188, v103
	v_add_f32_e32 v102, v118, v178
	v_add_f32_e32 v102, v212, v102
	v_add_f32_e32 v102, v119, v102
	v_add_f32_e32 v102, v188, v102
	v_fmamk_f32 v103, v120, 0x3dd53b94, v213
	s_waitcnt lgkmcnt(1)
	v_mfma_f32_32x32x16_bf16 v[66:81], v[98:101], v[150:153], v[66:81]
	v_exp_f32_e32 v120, v103
	v_fmamk_f32 v103, v104, 0x3dd53b94, v213
	v_exp_f32_e32 v189, v103
	v_fmamk_f32 v99, v121, 0x3dd53b94, v213
	ds_read_b128 v[178:181], v218 offset:49152
	ds_read_b128 v[182:185], v218 offset:57344
	v_exp_f32_e32 v121, v99
	v_fmamk_f32 v99, v105, 0x3dd53b94, v213
	s_waitcnt lgkmcnt(2)
	v_mfma_f32_32x32x16_bf16 v[82:97], v[114:117], v[150:153], v[82:97]
	v_exp_f32_e32 v190, v99
	v_add_f32_e32 v98, v120, v102
	v_add_f32_e32 v98, v189, v98
	v_add_f32_e32 v98, v121, v98
	v_add_f32_e32 v114, v190, v98
	v_fmamk_f32 v115, v122, 0x3dd53b94, v213
	v_exp_f32_e32 v122, v115
	s_waitcnt lgkmcnt(1)
	v_mfma_f32_32x32x16_bf16 v[66:81], v[178:181], v[154:157], v[66:81]
	v_fmamk_f32 v106, v106, 0x3dd53b94, v213
	v_exp_f32_e32 v191, v106
	v_add_f32_e32 v106, v122, v114
	v_fmamk_f32 v114, v123, 0x3dd53b94, v213
	ds_read_b128 v[98:101], v219 offset:49152
	ds_read_b128 v[102:105], v219 offset:57344
	v_exp_f32_e32 v123, v114
	v_fmamk_f32 v107, v107, 0x3dd53b94, v213
	s_waitcnt lgkmcnt(2)
	v_mfma_f32_32x32x16_bf16 v[82:97], v[182:185], v[154:157], v[82:97]
	v_exp_f32_e32 v192, v107
	v_add_f32_e32 v106, v191, v106
	v_add_f32_e32 v106, v123, v106
	v_add_f32_e32 v106, v192, v106
	v_fmamk_f32 v114, v124, 0x3dd53b94, v213
	s_waitcnt lgkmcnt(1)
	v_mfma_f32_32x32x16_bf16 v[66:81], v[98:101], v[158:161], v[66:81]
	v_add_u32_e32 v107, v211, v226
	v_exp_f32_e32 v124, v114
	v_fmamk_f32 v108, v108, 0x3dd53b94, v213
	v_exp_f32_e32 v193, v108
	ds_read_b128 v[98:101], v107
	ds_read_b128 v[114:117], v107 offset:4096
	v_fmamk_f32 v107, v125, 0x3dd53b94, v213
	v_exp_f32_e32 v125, v107
	s_waitcnt lgkmcnt(2)
	v_mfma_f32_32x32x16_bf16 v[82:97], v[102:105], v[158:161], v[82:97]
	v_fmamk_f32 v107, v109, 0x3dd53b94, v213
	v_exp_f32_e32 v218, v107
	v_add_f32_e32 v106, v124, v106
	v_add_f32_e32 v106, v193, v106
	v_add_f32_e32 v102, v125, v106
	v_add_f32_e32 v106, v218, v102
	v_fmamk_f32 v103, v126, 0x3dd53b94, v213
	s_waitcnt lgkmcnt(1)
	v_mfma_f32_32x32x16_bf16 v[66:81], v[98:101], v[162:165], v[66:81]
	v_exp_f32_e32 v126, v103
	v_fmamk_f32 v103, v110, 0x3dd53b94, v213
	v_add_u32_e32 v102, v211, v206
	v_exp_f32_e32 v219, v103
	v_fmamk_f32 v107, v127, 0x3dd53b94, v213
	ds_read_b128 v[98:101], v102
	ds_read_b128 v[102:105], v102 offset:4096
	v_exp_f32_e32 v127, v107
	s_waitcnt lgkmcnt(2)
	v_mfma_f32_32x32x16_bf16 v[82:97], v[114:117], v[162:165], v[82:97]
	v_fmamk_f32 v107, v111, 0x3dd53b94, v213
	v_exp_f32_e32 v239, v107
	v_add_f32_e32 v106, v126, v106
	v_add_f32_e32 v106, v219, v106
	v_add_f32_e32 v106, v127, v106
	v_add_f32_e32 v110, v239, v106
	v_fmamk_f32 v107, v128, 0x3dd53b94, v213
	s_waitcnt lgkmcnt(1)
	v_mfma_f32_32x32x16_bf16 v[66:81], v[98:101], v[166:169], v[66:81]
	v_exp_f32_e32 v114, v107
	v_fmamk_f32 v107, v112, 0x3dd53b94, v213
	v_add_u32_e32 v106, v211, v208
	v_exp_f32_e32 v115, v107
	v_fmamk_f32 v111, v129, 0x3dd53b94, v213
	ds_read_b128 v[98:101], v106
	ds_read_b128 v[106:109], v106 offset:4096
	v_exp_f32_e32 v116, v111
	s_waitcnt lgkmcnt(2)
	v_mfma_f32_32x32x16_bf16 v[82:97], v[102:105], v[166:169], v[82:97]
	v_fmac_f32_e32 v213, 0x3dd53b94, v113
	v_exp_f32_e32 v117, v213
	v_add_f32_e32 v110, v114, v110
	v_add_f32_e32 v110, v115, v110
	v_add_f32_e32 v102, v116, v110
	v_add_f32_e32 v128, v117, v102
	s_waitcnt lgkmcnt(1)
	v_mfma_f32_32x32x16_bf16 v[66:81], v[98:101], v[170:173], v[66:81]
	v_add_u32_e32 v110, v211, v223
	ds_read_b128 v[102:105], v110
	ds_read_b128 v[110:113], v110 offset:4096
	v_mov_b32_e32 v129, v128
	s_nop 1
	v_permlane32_swap_b32_e32 v128, v129
	v_add_f32_e32 v230, v128, v129
	v_cvt_pk_bf16_f32 v178, v220, v232
	s_waitcnt lgkmcnt(2)
	v_mfma_f32_32x32x16_bf16 v[82:97], v[106:109], v[170:173], v[82:97]
	v_cvt_pk_bf16_f32 v179, v210, v237
	v_cvt_pk_bf16_f32 v180, v118, v119
	v_cvt_pk_bf16_f32 v181, v120, v121
	v_cvt_pk_bf16_f32 v182, v122, v123
	v_cvt_pk_bf16_f32 v183, v124, v125
	v_cvt_pk_bf16_f32 v184, v126, v127
	v_cvt_pk_bf16_f32 v185, v114, v116
	v_fmac_f32_e32 v230, v233, v234
	v_permlane32_swap_b32_e32 v178, v180
	v_permlane32_swap_b32_e32 v179, v181
	v_permlane32_swap_b32_e32 v182, v184
	v_permlane32_swap_b32_e32 v183, v185
	s_waitcnt lgkmcnt(1)
	v_mfma_f32_32x32x16_bf16 v[66:81], v[102:105], v[174:177], v[66:81]
	v_cvt_pk_bf16_f32 v186, v221, v235
	v_cvt_pk_bf16_f32 v187, v236, v238
	v_cvt_pk_bf16_f32 v188, v212, v188
	v_cvt_pk_bf16_f32 v189, v189, v190
	v_cvt_pk_bf16_f32 v190, v191, v192
	v_cvt_pk_bf16_f32 v191, v193, v218
	v_cvt_pk_bf16_f32 v192, v219, v239
	s_waitcnt lgkmcnt(0)
	v_mfma_f32_32x32x16_bf16 v[82:97], v[110:113], v[174:177], v[82:97]
	v_cvt_pk_bf16_f32 v193, v115, v117
	v_permlane32_swap_b32_e32 v186, v188
	v_permlane32_swap_b32_e32 v187, v189
	v_permlane32_swap_b32_e32 v190, v192
	v_permlane32_swap_b32_e32 v191, v193
	v_cmp_gt_f32_e32 vcc, 1.0, v234
	s_cbranch_vccz .LBB0_962
